# P2 tile order rotated by 3 sections so q_a/K/V (attention inputs) are written last, for LLC residency at phase-3 start
# baseline (speedup 1.0000x reference)
.LBB0_221:
	s_add_u32 s0, s96, 0x26000000
	s_addc_u32 s1, s97, 0
	v_writelane_b32 v255, s0, 4
	s_nop 1
	v_writelane_b32 v255, s1, 5
	s_add_u32 s0, s96, 0x1f400000
	s_addc_u32 s1, s97, 0
	v_writelane_b32 v255, s0, 6
	s_cmp_lt_i32 s48, 3
	s_nop 0
	v_writelane_b32 v255, s1, 7
	s_cselect_b64 s[0:1], -1, 0
	s_cmp_gt_i32 s49, 2
	s_cselect_b64 s[2:3], -1, 0
	s_and_b64 s[0:1], s[0:1], s[2:3]
	s_andn2_b64 vcc, exec, s[0:1]
	s_cbranch_vccnz .LBB0_640
	s_cmpk_lt_i32 s73, 0x1200
	s_cselect_b64 s[0:1], -1, 0
	s_cmpk_gt_i32 s73, 0x11ff
	v_readfirstlane_b32 s2, v0
	s_cbranch_scc1 .LBB0_225
	s_ashr_i32 s3, s73, 31
	s_lshr_b32 s3, s3, 29
	s_add_i32 s3, s73, s3
	s_ashr_i32 s4, s3, 3
	s_and_b32 s3, s3, -8
	s_sub_i32 s3, s73, s3
	s_cmp_lt_i32 s3, 0
	s_movk_i32 s5, 0x241
	s_cselect_b32 s5, s5, 0x240
	s_mul_i32 s3, s3, s5
	s_add_i32 s3, s3, s4
	s_mul_hi_i32 s4, s3, 0x38e38e39
	s_lshr_b32 s5, s4, 31
	s_ashr_i32 s4, s4, 7
	s_add_i32 s4, s4, s5
	s_lshl_b32 s5, s4, 3
	s_mulk_i32 s4, 0x240
	s_sub_i32 s3, s3, s4
	s_sext_i32_i16 s4, s3
	s_bfe_u32 s4, s4, 0x3001c
	s_add_i32 s4, s3, s4
	s_sext_i32_i16 s6, s4
	s_and_b32 s4, s4, 0xfff8
	s_sub_i32 s3, s3, s4
	s_sext_i32_i16 s3, s3
	s_add_i32 s14, s5, s3
	s_ashr_i32 s12, s6, 3
	s_add_i32 s12, s12, 24
	s_cmp_lt_i32 s12, 0x48
	s_cbranch_scc1 .Lrot_ok1
	s_addk_i32 s12, 0xffb8
.Lrot_ok1:
	s_andn2_b64 vcc, exec, s[0:1]
	s_cbranch_vccz .LBB0_226

.LBB0_235:
	s_add_i32 s83, s83, 1
	s_mul_i32 s2, s83, s66
	s_mul_hi_u32 s3, s83, s72
	s_add_i32 s3, s3, s2
	s_mul_i32 s2, s83, s72
	v_readlane_b32 s8, v254, 55
	s_add_u32 s42, s2, s8
	s_addc_u32 s43, s3, s67
	v_mov_b64_e32 v[2:3], 0x1200
	v_cmp_lt_i64_e64 s[8:9], s[42:43], v[2:3]
	v_mov_b64_e32 v[2:3], 0x11ff
	v_cmp_gt_i64_e32 vcc, s[42:43], v[2:3]
	s_cbranch_vccnz .LBB0_237
	s_ashr_i32 s2, s42, 31
	s_lshr_b32 s2, s2, 29
	s_add_i32 s2, s42, s2
	s_ashr_i32 s3, s2, 3
	s_and_b32 s2, s2, -8
	s_sub_i32 s2, s42, s2
	s_cmp_lt_i32 s2, 0
	s_movk_i32 s13, 0x241
	s_cselect_b32 s13, s13, 0x240
	s_mul_i32 s2, s2, s13
	s_add_i32 s2, s2, s3
	s_mul_hi_i32 s3, s2, 0x38e38e39
	s_lshr_b32 s13, s3, 31
	s_ashr_i32 s3, s3, 7
	s_add_i32 s3, s3, s13
	s_lshl_b32 s13, s3, 3
	s_sub_i32 s15, 64, s13
	s_min_i32 s15, s15, 8
	s_abs_i32 s20, s15
	v_cvt_f32_u32_e32 v2, s20
	s_sub_i32 s29, 0, s20
	s_mulk_i32 s3, 0x240
	s_sub_i32 s2, s2, s3
	v_rcp_iflag_f32_e32 v2, v2
	s_abs_i32 s3, s2
	s_xor_b32 s28, s2, s15
	s_ashr_i32 s28, s28, 31
	v_mul_f32_e32 v2, 0x4f7ffffe, v2
	v_cvt_u32_f32_e32 v2, v2
	s_nop 0
	v_readfirstlane_b32 s33, v2
	s_mul_i32 s29, s29, s33
	s_mul_hi_u32 s29, s33, s29
	s_add_i32 s33, s33, s29
	s_mul_hi_u32 s29, s3, s33
	s_mul_i32 s33, s29, s20
	s_sub_i32 s3, s3, s33
	s_add_i32 s38, s29, 1
	s_sub_i32 s33, s3, s20
	s_cmp_ge_u32 s3, s20
	s_cselect_b32 s29, s38, s29
	s_cselect_b32 s3, s33, s3
	s_add_i32 s33, s29, 1
	s_cmp_ge_u32 s3, s20
	s_cselect_b32 s3, s33, s29
	s_xor_b32 s3, s3, s28
	s_sub_i32 s38, s3, s28
	s_mul_i32 s3, s38, s15
	s_sub_i32 s2, s2, s3
	s_add_i32 s16, s13, s2
	s_add_i32 s38, s38, 24
	s_cmp_lt_i32 s38, 0x48
	s_cbranch_scc1 .Lrot_ok2
	s_addk_i32 s38, 0xffb8
.Lrot_ok2:
.LBB0_237:
	s_ashr_i32 s17, s16, 31
	s_lshl_b64 s[2:3], s[16:17], 19
	v_readlane_b32 s28, v255, 6
	v_readlane_b32 s29, v255, 7
	s_add_u32 s18, s28, s2
	s_addc_u32 s19, s29, s3
	s_and_b64 s[2:3], s[8:9], exec
	s_cselect_b32 s2, s19, s11
	s_cselect_b32 s3, s18, s10
	s_ashr_i32 s39, s38, 31
	s_lshl_b64 s[28:29], s[38:39], 19
	s_add_u32 s70, s37, s28
	s_addc_u32 s71, s56, s29
	s_and_b64 s[28:29], s[8:9], exec
	s_cselect_b32 s13, s71, s47
	s_cselect_b32 s15, s70, s46
	s_add_u32 s10, s10, 0x40080
	s_addc_u32 s11, s11, 0
	s_add_u32 s20, s46, 0x100
	v_mov_b32_e32 v2, 0
	s_addc_u32 s33, s47, 0
	s_mov_b32 s39, -2
	v_mov_b32_e32 v3, v2
	v_mov_b32_e32 v4, v2
	v_mov_b32_e32 v5, v2
	v_mov_b32_e32 v6, v2
	v_mov_b32_e32 v7, v2
	v_mov_b32_e32 v8, v2
	v_mov_b32_e32 v9, v2
	v_mov_b32_e32 v26, v2
	v_mov_b32_e32 v27, v2
	v_mov_b32_e32 v28, v2
	v_mov_b32_e32 v29, v2
	v_mov_b32_e32 v30, v2
	v_mov_b32_e32 v31, v2
	v_mov_b32_e32 v32, v2
	v_mov_b32_e32 v33, v2
	v_mov_b32_e32 v50, v2
	v_mov_b32_e32 v51, v2
	v_mov_b32_e32 v52, v2
	v_mov_b32_e32 v53, v2
	v_mov_b32_e32 v54, v2
	v_mov_b32_e32 v55, v2
	v_mov_b32_e32 v56, v2
	v_mov_b32_e32 v57, v2
	v_mov_b32_e32 v66, v2
	v_mov_b32_e32 v67, v2
	v_mov_b32_e32 v68, v2
	v_mov_b32_e32 v69, v2
	v_mov_b32_e32 v70, v2
	v_mov_b32_e32 v71, v2
	v_mov_b32_e32 v72, v2
	v_mov_b32_e32 v73, v2
	v_mov_b32_e32 v10, v2
	v_mov_b32_e32 v11, v2
	v_mov_b32_e32 v12, v2
	v_mov_b32_e32 v13, v2
	v_mov_b32_e32 v14, v2
	v_mov_b32_e32 v15, v2
	v_mov_b32_e32 v16, v2
	v_mov_b32_e32 v17, v2
	v_mov_b32_e32 v42, v2
	v_mov_b32_e32 v43, v2
	v_mov_b32_e32 v44, v2
	v_mov_b32_e32 v45, v2
	v_mov_b32_e32 v46, v2
	v_mov_b32_e32 v47, v2
	v_mov_b32_e32 v48, v2
	v_mov_b32_e32 v49, v2
	v_mov_b32_e32 v58, v2
	v_mov_b32_e32 v59, v2
	v_mov_b32_e32 v60, v2
	v_mov_b32_e32 v61, v2
	v_mov_b32_e32 v62, v2
	v_mov_b32_e32 v63, v2
	v_mov_b32_e32 v64, v2
	v_mov_b32_e32 v65, v2
	v_mov_b32_e32 v74, v2
	v_mov_b32_e32 v75, v2
	v_mov_b32_e32 v76, v2
	v_mov_b32_e32 v77, v2
	v_mov_b32_e32 v78, v2
	v_mov_b32_e32 v79, v2
	v_mov_b32_e32 v80, v2
	v_mov_b32_e32 v81, v2
	v_mov_b32_e32 v82, v2
	v_mov_b32_e32 v83, v2
	v_mov_b32_e32 v84, v2
	v_mov_b32_e32 v85, v2
	v_mov_b32_e32 v86, v2
	v_mov_b32_e32 v87, v2
	v_mov_b32_e32 v88, v2
	v_mov_b32_e32 v89, v2
	v_mov_b32_e32 v98, v2
	v_mov_b32_e32 v99, v2
	v_mov_b32_e32 v100, v2
	v_mov_b32_e32 v101, v2
	v_mov_b32_e32 v102, v2
	v_mov_b32_e32 v103, v2
	v_mov_b32_e32 v104, v2
	v_mov_b32_e32 v105, v2
	v_mov_b32_e32 v114, v2
	v_mov_b32_e32 v115, v2
	v_mov_b32_e32 v116, v2
	v_mov_b32_e32 v117, v2
	v_mov_b32_e32 v118, v2
	v_mov_b32_e32 v119, v2
	v_mov_b32_e32 v120, v2
	v_mov_b32_e32 v121, v2
	v_mov_b32_e32 v130, v2
	v_mov_b32_e32 v131, v2
	v_mov_b32_e32 v132, v2
	v_mov_b32_e32 v133, v2
	v_mov_b32_e32 v134, v2
	v_mov_b32_e32 v135, v2
	v_mov_b32_e32 v136, v2
	v_mov_b32_e32 v137, v2
	v_mov_b32_e32 v90, v2
	v_mov_b32_e32 v91, v2
	v_mov_b32_e32 v92, v2
	v_mov_b32_e32 v93, v2
	v_mov_b32_e32 v94, v2
	v_mov_b32_e32 v95, v2
	v_mov_b32_e32 v96, v2
	v_mov_b32_e32 v97, v2
	v_mov_b32_e32 v106, v2
	v_mov_b32_e32 v107, v2
	v_mov_b32_e32 v108, v2
	v_mov_b32_e32 v109, v2
	v_mov_b32_e32 v110, v2
	v_mov_b32_e32 v111, v2
	v_mov_b32_e32 v112, v2
	v_mov_b32_e32 v113, v2
	v_mov_b32_e32 v122, v2
	v_mov_b32_e32 v123, v2
	v_mov_b32_e32 v124, v2
	v_mov_b32_e32 v125, v2
	v_mov_b32_e32 v126, v2
	v_mov_b32_e32 v127, v2
	v_mov_b32_e32 v128, v2
	v_mov_b32_e32 v129, v2
	v_mov_b32_e32 v138, v2
	v_mov_b32_e32 v139, v2
	v_mov_b32_e32 v140, v2
	v_mov_b32_e32 v141, v2
	v_mov_b32_e32 v142, v2
	v_mov_b32_e32 v143, v2
	v_mov_b32_e32 v144, v2
	v_mov_b32_e32 v145, v2
